# instruction selection: the 32 f32 multiplies of the attention-hosted fp6 conversion done as 16 packed v_pk_mul_f32; loop-edge hoist also applied to the bf16 out-projection GEMM loop
# speedup vs baseline: 1.0023x; 1.0023x over previous
; #define PG8_STAGE(bufoff, gbase, voff) do { _Pragma("unroll") for (int _i = 0; _i < 2; ++_i) \
;         __builtin_amdgcn_global_load_lds((const unsigned*)((const char*)(gbase) + (voff)[_i]), (LAS unsigned*)(lds + (bufoff) + ldsw + _i * 8192), 16, 0, 0); } while (0)
; #define PG8_LDA(dst, b, h) do { _Pragma("unroll") for (int m = 0; m < 4; ++m) _Pragma("unroll") for (int k = 0; k < 2; ++k) dst[m][k] = *(const LAS bf16x8*)(lds + PG8_SA(b, h) + aoff + m * 2048 + k * 1024); } while (0)
; #define PG8_LDB(dst, b, h) do { _Pragma("unroll") for (int n = 0; n < 2; ++n) _Pragma("unroll") for (int k = 0; k < 2; ++k) dst[n][k] = *(const LAS bf16x8*)(lds + PG8_SB(b, h) + boff + n * 2048 + k * 1024); } while (0)
; #define PG8_MMA(ai, bj, At, Bt) do { __builtin_amdgcn_s_setprio(1); _Pragma("unroll") for (int m = 0; m < 4; ++m) _Pragma("unroll") for (int n = 0; n < 2; ++n) _Pragma("unroll") for (int k = 0; k < 2; ++k) \
;         acc[ai][bj][m][n] = __builtin_amdgcn_mfma_f32_16x16x32_bf16(Bt[n][k], At[m][k], acc[ai][bj][m][n], 0, 0, 0); __builtin_amdgcn_s_setprio(0); } while (0)
; #define PG8_WAIT_V(n) asm volatile("s_waitcnt vmcnt(" #n ")" ::: "memory")
; #define PG8_WAIT_L(n) asm volatile("s_waitcnt lgkmcnt(" #n ")" ::: "memory")
; #define PG8_BAR __builtin_amdgcn_s_barrier()
; template <class Epi, class Sched>
; __device__ __forceinline__ void gemm_phase(LAS unsigned char* lds, const Gemm g, const Sched& S, const Epi& E) {
;     ...
;         for (int t = 0; t < nt; t += 2) {
;             const bool last = (t == nt - 2);
;             const char* a1 = cA + (size_t)(t + 1) * kstep;
;             const char* a2 = last ? nA : cA + (size_t)(t + 2) * kstep; const char* b2 = last ? nB : cB + (size_t)(t + 2) * kstep;
;             const char* a3 = a2 + kstep; const char* b3 = b2 + kstep;
;             if (last && has_next) S.a_ready(nxt);
;             PG8_LDB(B0, 0, 0); PG8_LDB(B1, 0, 1); PG8_SCHED; PG8_LDA(At, 0, 0); PG8_STAGE(PG8_SA(1, 1), a1 + hstepA, voffA);
;             PG8_WAIT_V(8); PG8_WAIT_L(0); PG8_BAR; PG8_MMA(0, 0, At, B0); PG8_MMA(0, 1, At, B1); PG8_BAR; PG8_SCHED;
;             PG8_LDA(At, 0, 1); PG8_STAGE(PG8_SB(0, 0), b2, voffB); PG8_STAGE(PG8_SB(0, 1), b2 + hstepB, voffB); PG8_STAGE(PG8_SA(0, 0), a2, voffA);
;             PG8_WAIT_V(8); PG8_WAIT_L(0); PG8_BAR; PG8_MMA(1, 0, At, B0); PG8_MMA(1, 1, At, B1); PG8_BAR; PG8_SCHED;
.LBB0_469:
	ds_read_b128 v[130:133], v191
	ds_read_b128 v[134:137], v191 offset:1024
	ds_read_b128 v[138:141], v191 offset:2048
	ds_read_b128 v[142:145], v191 offset:3072
	ds_read_b128 v[146:149], v192
	ds_read_b128 v[150:153], v192 offset:1024
	ds_read_b128 v[154:157], v192 offset:2048
	ds_read_b128 v[158:161], v192 offset:3072
	s_add_u32 s8, s60, 0xfff80080
	s_addc_u32 s9, s61, -1
	s_cmp_eq_u32 s82, 28
	s_cselect_b32 s65, s45, s9
	s_cselect_b32 s64, s47, s8
	s_cselect_b32 s63, s73, s81
	s_cselect_b32 s62, s74, s75
	v_lshl_add_u64 v[186:187], s[60:61], 0, v[166:167]
	s_add_i32 m0, s11, 0xc000
	ds_read_b128 v[174:177], v193
	ds_read_b128 v[178:181], v193 offset:1024
	ds_read_b128 v[182:185], v193 offset:2048
	ds_read_b128 v[194:197], v193 offset:3072
	ds_read_b128 v[198:201], v193 offset:4096
	ds_read_b128 v[202:205], v193 offset:5120
	ds_read_b128 v[206:209], v193 offset:6144
	ds_read_b128 v[210:213], v193 offset:7168
	global_load_lds_dwordx4 v[186:187], off
	v_lshl_add_u64 v[186:187], s[60:61], 0, v[168:169]
	s_add_i32 m0, s11, 0xe000
	s_nop 0
	global_load_lds_dwordx4 v[186:187], off
	s_waitcnt vmcnt(8)
	s_waitcnt lgkmcnt(0)
	s_barrier
	s_setprio 1
	v_mfma_f32_16x16x32_bf16 v[126:129], v[130:133], v[174:177], v[126:129]
	v_mfma_f32_16x16x32_bf16 v[122:125], v[138:141], v[174:177], v[122:125]
	v_mfma_f32_16x16x32_bf16 v[118:121], v[130:133], v[182:185], v[118:121]
	v_mfma_f32_16x16x32_bf16 v[114:117], v[138:141], v[182:185], v[114:117]
	v_mfma_f32_16x16x32_bf16 v[94:97], v[130:133], v[198:201], v[94:97]
	v_mfma_f32_16x16x32_bf16 v[90:93], v[138:141], v[198:201], v[90:93]
	v_mfma_f32_16x16x32_bf16 v[86:89], v[130:133], v[206:209], v[86:89]
	v_mfma_f32_16x16x32_bf16 v[82:85], v[138:141], v[206:209], v[82:85]
	v_mfma_f32_16x16x32_bf16 v[126:129], v[134:137], v[178:181], v[126:129]
	v_mfma_f32_16x16x32_bf16 v[122:125], v[142:145], v[178:181], v[122:125]
	v_mfma_f32_16x16x32_bf16 v[118:121], v[134:137], v[194:197], v[118:121]
	v_mfma_f32_16x16x32_bf16 v[114:117], v[142:145], v[194:197], v[114:117]
	v_mfma_f32_16x16x32_bf16 v[94:97], v[134:137], v[202:205], v[94:97]
	v_mfma_f32_16x16x32_bf16 v[90:93], v[142:145], v[202:205], v[90:93]
	v_mfma_f32_16x16x32_bf16 v[86:89], v[134:137], v[210:213], v[86:89]
	v_mfma_f32_16x16x32_bf16 v[82:85], v[142:145], v[210:213], v[82:85]
	s_setprio 0
	s_setprio 1
	v_mfma_f32_16x16x32_bf16 v[110:113], v[146:149], v[174:177], v[110:113]
	v_mfma_f32_16x16x32_bf16 v[106:109], v[154:157], v[174:177], v[106:109]
	v_mfma_f32_16x16x32_bf16 v[102:105], v[146:149], v[182:185], v[102:105]
	v_mfma_f32_16x16x32_bf16 v[98:101], v[154:157], v[182:185], v[98:101]
	v_mfma_f32_16x16x32_bf16 v[78:81], v[146:149], v[198:201], v[78:81]
	v_mfma_f32_16x16x32_bf16 v[74:77], v[154:157], v[198:201], v[74:77]
	v_mfma_f32_16x16x32_bf16 v[70:73], v[146:149], v[206:209], v[70:73]
	v_mfma_f32_16x16x32_bf16 v[66:69], v[154:157], v[206:209], v[66:69]
	v_mfma_f32_16x16x32_bf16 v[110:113], v[150:153], v[178:181], v[110:113]
	v_mfma_f32_16x16x32_bf16 v[106:109], v[158:161], v[178:181], v[106:109]
	v_mfma_f32_16x16x32_bf16 v[102:105], v[150:153], v[194:197], v[102:105]
	v_mfma_f32_16x16x32_bf16 v[98:101], v[158:161], v[194:197], v[98:101]
	v_mfma_f32_16x16x32_bf16 v[78:81], v[150:153], v[202:205], v[78:81]
	v_mfma_f32_16x16x32_bf16 v[74:77], v[158:161], v[202:205], v[74:77]
	v_mfma_f32_16x16x32_bf16 v[70:73], v[150:153], v[210:213], v[70:73]
	v_mfma_f32_16x16x32_bf16 v[66:69], v[158:161], v[210:213], v[66:69]
	s_setprio 0
	s_barrier
	s_add_i32 s8, s79, s10
	v_lshl_add_u64 v[186:187], s[62:63], 0, v[164:165]
	s_mov_b32 m0, s8
	ds_read_b128 v[174:177], v193 offset:16384
	ds_read_b128 v[178:181], v193 offset:17408
	ds_read_b128 v[182:185], v193 offset:18432
	ds_read_b128 v[194:197], v193 offset:19456
	ds_read_b128 v[198:201], v193 offset:20480
	ds_read_b128 v[202:205], v193 offset:21504
	ds_read_b128 v[206:209], v193 offset:22528
	ds_read_b128 v[210:213], v193 offset:23552
	global_load_lds_dwordx4 v[186:187], off
	s_add_i32 m0, s8, 0x2000
	s_add_u32 s8, s62, 0x80000
	v_lshl_add_u64 v[214:215], s[62:63], 0, v[162:163]
	s_addc_u32 s9, s63, 0
	s_add_i32 s12, s80, s10
	global_load_lds_dwordx4 v[214:215], off
	v_lshl_add_u64 v[216:217], s[8:9], 0, v[164:165]
	s_mov_b32 m0, s12
	v_lshl_add_u64 v[218:219], s[64:65], 0, v[162:163]
	global_load_lds_dwordx4 v[216:217], off
	v_lshl_add_u64 v[216:217], s[8:9], 0, v[162:163]
	s_add_i32 m0, s12, 0x2000
	s_nop 0
	global_load_lds_dwordx4 v[216:217], off
	v_lshl_add_u64 v[216:217], s[64:65], 0, v[164:165]
	s_mov_b32 m0, s11
	s_nop 0
	global_load_lds_dwordx4 v[216:217], off
	s_mov_b32 m0, s24
	s_nop 0
	global_load_lds_dwordx4 v[218:219], off
	s_waitcnt vmcnt(8)
	s_waitcnt lgkmcnt(0)
	s_barrier
; #define PG8_STAGE(bufoff, gbase, voff) do { _Pragma("unroll") for (int _i = 0; _i < 2; ++_i) \
;         __builtin_amdgcn_global_load_lds((const unsigned*)((const char*)(gbase) + (voff)[_i]), (LAS unsigned*)(lds + (bufoff) + ldsw + _i * 8192), 16, 0, 0); } while (0)
; #define PG8_LDA(dst, b, h) do { _Pragma("unroll") for (int m = 0; m < 4; ++m) _Pragma("unroll") for (int k = 0; k < 2; ++k) dst[m][k] = *(const LAS bf16x8*)(lds + PG8_SA(b, h) + aoff + m * 2048 + k * 1024); } while (0)
; #define PG8_LDB(dst, b, h) do { _Pragma("unroll") for (int n = 0; n < 2; ++n) _Pragma("unroll") for (int k = 0; k < 2; ++k) dst[n][k] = *(const LAS bf16x8*)(lds + PG8_SB(b, h) + boff + n * 2048 + k * 1024); } while (0)
; #define PG8_MMA(ai, bj, At, Bt) do { __builtin_amdgcn_s_setprio(1); _Pragma("unroll") for (int m = 0; m < 4; ++m) _Pragma("unroll") for (int n = 0; n < 2; ++n) _Pragma("unroll") for (int k = 0; k < 2; ++k) \
;         acc[ai][bj][m][n] = __builtin_amdgcn_mfma_f32_16x16x32_bf16(Bt[n][k], At[m][k], acc[ai][bj][m][n], 0, 0, 0); __builtin_amdgcn_s_setprio(0); } while (0)
; #define PG8_WAIT_V(n) asm volatile("s_waitcnt vmcnt(" #n ")" ::: "memory")
; #define PG8_WAIT_L(n) asm volatile("s_waitcnt lgkmcnt(" #n ")" ::: "memory")
; #define PG8_BAR __builtin_amdgcn_s_barrier()
; #define PG8_SCHED __builtin_amdgcn_sched_barrier(0)
; #define PG8_STAGE(bufoff, gbase, voff) do { _Pragma("unroll") for (int _i = 0; _i < 2; ++_i) \
;         __builtin_amdgcn_global_load_lds((const unsigned*)((const char*)(gbase) + (voff)[_i]), (LAS unsigned*)(lds + (bufoff) + ldsw + _i * 8192), 16, 0, 0); } while (0)
; #define PG8_LDA(dst, b, h) do { _Pragma("unroll") for (int m = 0; m < 4; ++m) PG8_LD1(dst[m], PG8_SA(b, h) + aoff0 + m * 2048, PG8_SA(b, h) + aoff1 + m * 2048); } while (0)
; #define PG8_WAIT_V(n) asm volatile("s_waitcnt vmcnt(" #n ")" ::: "memory")
; template <class Epi, class Sched>
; __device__ __forceinline__ void gemm_phase(LAS unsigned char* lds, const Gemm g, const Sched& S, const Epi& E) {
;     ...
;             PG8_WAIT_V(8); PG8_WAIT_L(0); PG8_BAR; PG8_MMA(1, 0, At, B0); PG8_MMA(1, 1, At, B1); PG8_BAR; PG8_SCHED;
;             PG8_LDB(B0, 1, 0); PG8_LDB(B1, 1, 1); PG8_SCHED; PG8_LDA(At, 1, 0); PG8_STAGE(PG8_SA(0, 1), a2 + hstepA, voffA);
;             PG8_WAIT_V(8); PG8_WAIT_L(0); PG8_BAR; PG8_MMA(0, 0, At, B0); PG8_MMA(0, 1, At, B1); PG8_BAR; PG8_SCHED;
	s_setprio 1
	v_mfma_f32_16x16x32_bf16 v[62:65], v[130:133], v[174:177], v[62:65]
	v_mfma_f32_16x16x32_bf16 v[58:61], v[138:141], v[174:177], v[58:61]
	v_mfma_f32_16x16x32_bf16 v[54:57], v[130:133], v[182:185], v[54:57]
	v_mfma_f32_16x16x32_bf16 v[42:45], v[138:141], v[182:185], v[42:45]
	v_mfma_f32_16x16x32_bf16 v[38:41], v[130:133], v[198:201], v[38:41]
	v_mfma_f32_16x16x32_bf16 v[26:29], v[138:141], v[198:201], v[26:29]
	v_mfma_f32_16x16x32_bf16 v[22:25], v[130:133], v[206:209], v[22:25]
	v_mfma_f32_16x16x32_bf16 v[10:13], v[138:141], v[206:209], v[10:13]
	v_mfma_f32_16x16x32_bf16 v[62:65], v[134:137], v[178:181], v[62:65]
	v_mfma_f32_16x16x32_bf16 v[58:61], v[142:145], v[178:181], v[58:61]
	v_mfma_f32_16x16x32_bf16 v[54:57], v[134:137], v[194:197], v[54:57]
	v_mfma_f32_16x16x32_bf16 v[42:45], v[142:145], v[194:197], v[42:45]
	v_mfma_f32_16x16x32_bf16 v[38:41], v[134:137], v[202:205], v[38:41]
	v_mfma_f32_16x16x32_bf16 v[26:29], v[142:145], v[202:205], v[26:29]
	v_mfma_f32_16x16x32_bf16 v[22:25], v[134:137], v[210:213], v[22:25]
	v_mfma_f32_16x16x32_bf16 v[10:13], v[142:145], v[210:213], v[10:13]
	s_setprio 0
	s_setprio 1
	v_mfma_f32_16x16x32_bf16 v[50:53], v[146:149], v[174:177], v[50:53]
	v_mfma_f32_16x16x32_bf16 v[46:49], v[154:157], v[174:177], v[46:49]
	v_mfma_f32_16x16x32_bf16 v[34:37], v[146:149], v[182:185], v[34:37]
	v_mfma_f32_16x16x32_bf16 v[30:33], v[154:157], v[182:185], v[30:33]
	v_mfma_f32_16x16x32_bf16 v[18:21], v[146:149], v[198:201], v[18:21]
	v_mfma_f32_16x16x32_bf16 v[14:17], v[154:157], v[198:201], v[14:17]
	v_mfma_f32_16x16x32_bf16 v[6:9], v[146:149], v[206:209], v[6:9]
	v_mfma_f32_16x16x32_bf16 v[2:5], v[154:157], v[206:209], v[2:5]
	v_mfma_f32_16x16x32_bf16 v[50:53], v[150:153], v[178:181], v[50:53]
	v_mfma_f32_16x16x32_bf16 v[46:49], v[158:161], v[178:181], v[46:49]
	v_mfma_f32_16x16x32_bf16 v[34:37], v[150:153], v[194:197], v[34:37]
	v_mfma_f32_16x16x32_bf16 v[30:33], v[158:161], v[194:197], v[30:33]
	v_mfma_f32_16x16x32_bf16 v[18:21], v[150:153], v[202:205], v[18:21]
	v_mfma_f32_16x16x32_bf16 v[14:17], v[158:161], v[202:205], v[14:17]
	v_mfma_f32_16x16x32_bf16 v[6:9], v[150:153], v[210:213], v[6:9]
	v_mfma_f32_16x16x32_bf16 v[2:5], v[158:161], v[210:213], v[2:5]
	s_setprio 0
	s_barrier
	s_add_i32 s12, 0, 0x18000
	s_add_i32 s13, 0, 0x1c000
	v_add_u32_e32 v142, s12, v189
	v_add_u32_e32 v158, s13, v189
	ds_read_b128 v[130:133], v142
	ds_read_b128 v[134:137], v142 offset:1024
	ds_read_b128 v[138:141], v142 offset:2048
	ds_read_b128 v[142:145], v142 offset:3072
	ds_read_b128 v[146:149], v158
	ds_read_b128 v[150:153], v158 offset:1024
	ds_read_b128 v[154:157], v158 offset:2048
	ds_read_b128 v[158:161], v158 offset:3072
	s_add_u32 s8, s64, 0x80000
	s_addc_u32 s9, s65, 0
	s_mov_b32 m0, s25
	v_lshl_add_u64 v[220:221], s[8:9], 0, v[164:165]
	ds_read_b128 v[174:177], v193 offset:32768
	ds_read_b128 v[178:181], v193 offset:33792
	ds_read_b128 v[182:185], v193 offset:34816
	ds_read_b128 v[194:197], v193 offset:35840
	ds_read_b128 v[198:201], v193 offset:36864
	ds_read_b128 v[202:205], v193 offset:37888
	ds_read_b128 v[206:209], v193 offset:38912
	ds_read_b128 v[210:213], v193 offset:39936
	global_load_lds_dwordx4 v[220:221], off
	v_lshl_add_u64 v[220:221], s[8:9], 0, v[162:163]
	s_mov_b32 m0, s33
	s_nop 0
	global_load_lds_dwordx4 v[220:221], off
	s_waitcnt vmcnt(8)
	s_waitcnt lgkmcnt(0)
	s_barrier
	s_setprio 1
	v_mfma_f32_16x16x32_bf16 v[126:129], v[130:133], v[174:177], v[126:129]
	v_mfma_f32_16x16x32_bf16 v[122:125], v[138:141], v[174:177], v[122:125]
	v_mfma_f32_16x16x32_bf16 v[118:121], v[130:133], v[182:185], v[118:121]
	v_mfma_f32_16x16x32_bf16 v[114:117], v[138:141], v[182:185], v[114:117]
	v_mfma_f32_16x16x32_bf16 v[94:97], v[130:133], v[198:201], v[94:97]
	v_mfma_f32_16x16x32_bf16 v[90:93], v[138:141], v[198:201], v[90:93]
	v_mfma_f32_16x16x32_bf16 v[86:89], v[130:133], v[206:209], v[86:89]
	v_mfma_f32_16x16x32_bf16 v[82:85], v[138:141], v[206:209], v[82:85]
	v_mfma_f32_16x16x32_bf16 v[126:129], v[134:137], v[178:181], v[126:129]
	v_mfma_f32_16x16x32_bf16 v[122:125], v[142:145], v[178:181], v[122:125]
	v_mfma_f32_16x16x32_bf16 v[118:121], v[134:137], v[194:197], v[118:121]
	v_mfma_f32_16x16x32_bf16 v[114:117], v[142:145], v[194:197], v[114:117]
	v_mfma_f32_16x16x32_bf16 v[94:97], v[134:137], v[202:205], v[94:97]
	v_mfma_f32_16x16x32_bf16 v[90:93], v[142:145], v[202:205], v[90:93]
	v_mfma_f32_16x16x32_bf16 v[86:89], v[134:137], v[210:213], v[86:89]
	v_mfma_f32_16x16x32_bf16 v[82:85], v[142:145], v[210:213], v[82:85]
	s_setprio 0
	s_setprio 1
	v_mfma_f32_16x16x32_bf16 v[110:113], v[146:149], v[174:177], v[110:113]
	v_mfma_f32_16x16x32_bf16 v[106:109], v[154:157], v[174:177], v[106:109]
	v_mfma_f32_16x16x32_bf16 v[102:105], v[146:149], v[182:185], v[102:105]
	v_mfma_f32_16x16x32_bf16 v[98:101], v[154:157], v[182:185], v[98:101]
	v_mfma_f32_16x16x32_bf16 v[78:81], v[146:149], v[198:201], v[78:81]
	v_mfma_f32_16x16x32_bf16 v[74:77], v[154:157], v[198:201], v[74:77]
	v_mfma_f32_16x16x32_bf16 v[70:73], v[146:149], v[206:209], v[70:73]
	v_mfma_f32_16x16x32_bf16 v[66:69], v[154:157], v[206:209], v[66:69]
	v_mfma_f32_16x16x32_bf16 v[110:113], v[150:153], v[178:181], v[110:113]
	v_mfma_f32_16x16x32_bf16 v[106:109], v[158:161], v[178:181], v[106:109]
	v_mfma_f32_16x16x32_bf16 v[102:105], v[150:153], v[194:197], v[102:105]
	v_mfma_f32_16x16x32_bf16 v[98:101], v[158:161], v[194:197], v[98:101]
	v_mfma_f32_16x16x32_bf16 v[78:81], v[150:153], v[202:205], v[78:81]
	v_mfma_f32_16x16x32_bf16 v[74:77], v[158:161], v[202:205], v[74:77]
	v_mfma_f32_16x16x32_bf16 v[70:73], v[150:153], v[210:213], v[70:73]
	v_mfma_f32_16x16x32_bf16 v[66:69], v[158:161], v[210:213], v[66:69]
	s_setprio 0
	s_barrier
; #define PG8_STAGE(bufoff, gbase, voff) do { _Pragma("unroll") for (int _i = 0; _i < 2; ++_i) \
;         __builtin_amdgcn_global_load_lds((const unsigned*)((const char*)(gbase) + (voff)[_i]), (LAS unsigned*)(lds + (bufoff) + ldsw + _i * 8192), 16, 0, 0); } while (0)
; #define PG8_LDA(dst, b, h) do { _Pragma("unroll") for (int m = 0; m < 4; ++m) _Pragma("unroll") for (int k = 0; k < 2; ++k) dst[m][k] = *(const LAS bf16x8*)(lds + PG8_SA(b, h) + aoff + m * 2048 + k * 1024); } while (0)
; #define PG8_MMA(ai, bj, At, Bt) do { __builtin_amdgcn_s_setprio(1); _Pragma("unroll") for (int m = 0; m < 4; ++m) _Pragma("unroll") for (int n = 0; n < 2; ++n) _Pragma("unroll") for (int k = 0; k < 2; ++k) \
;         acc[ai][bj][m][n] = __builtin_amdgcn_mfma_f32_16x16x32_bf16(Bt[n][k], At[m][k], acc[ai][bj][m][n], 0, 0, 0); __builtin_amdgcn_s_setprio(0); } while (0)
; #define PG8_WAIT_V(n) asm volatile("s_waitcnt vmcnt(" #n ")" ::: "memory")
; #define PG8_WAIT_L(n) asm volatile("s_waitcnt lgkmcnt(" #n ")" ::: "memory")
; #define PG8_BAR __builtin_amdgcn_s_barrier()
; #define PG8_SCHED __builtin_amdgcn_sched_barrier(0)
; #define PG8_STAGE(bufoff, gbase, voff) do { _Pragma("unroll") for (int _i = 0; _i < 2; ++_i) \
;         __builtin_amdgcn_global_load_lds((const unsigned*)((const char*)(gbase) + (voff)[_i]), (LAS unsigned*)(lds + (bufoff) + ldsw + _i * 8192), 16, 0, 0); } while (0)
; #define PG8_LDA(dst, b, h) do { _Pragma("unroll") for (int m = 0; m < 4; ++m) PG8_LD1(dst[m], PG8_SA(b, h) + aoff0 + m * 2048, PG8_SA(b, h) + aoff1 + m * 2048); } while (0)
; #define PG8_WAIT_V(n) asm volatile("s_waitcnt vmcnt(" #n ")" ::: "memory")
; #define PG8_WAIT_L(n) asm volatile("s_waitcnt lgkmcnt(" #n ")" ::: "memory")
; #define PG8_BAR __builtin_amdgcn_s_barrier()
; #define PG8_SCHED __builtin_amdgcn_sched_barrier(0)
; template <class Epi, class Sched>
; __device__ __forceinline__ void gemm_phase(LAS unsigned char* lds, const Gemm g, const Sched& S, const Epi& E) {
;     ...
;             PG8_LDA(At, 1, 1); PG8_STAGE(PG8_SB(1, 0), b3, voffB); PG8_STAGE(PG8_SB(1, 1), b3 + hstepB, voffB); PG8_STAGE(PG8_SA(1, 0), a3, voffA);
;             PG8_WAIT_V(8); PG8_WAIT_L(0); PG8_BAR; PG8_MMA(1, 0, At, B0); PG8_MMA(1, 1, At, B1); PG8_BAR; PG8_SCHED;
;         }
;         if (wr == 0) PG8_BAR;
	s_add_i32 s8, s12, s10
	v_lshl_add_u64 v[186:187], v[186:187], 0, s[38:39]
	s_mov_b32 m0, s8
	ds_read_b128 v[174:177], v193 offset:49152
	ds_read_b128 v[178:181], v193 offset:50176
	ds_read_b128 v[182:185], v193 offset:51200
	ds_read_b128 v[194:197], v193 offset:52224
	ds_read_b128 v[198:201], v193 offset:53248
	ds_read_b128 v[202:205], v193 offset:54272
	ds_read_b128 v[206:209], v193 offset:55296
	ds_read_b128 v[210:213], v193 offset:56320
	global_load_lds_dwordx4 v[186:187], off
	s_add_i32 m0, s8, 0x2000
	s_add_u32 s8, s62, 0x80080
	v_lshl_add_u64 v[186:187], v[214:215], 0, s[38:39]
	s_addc_u32 s9, s63, 0
	s_add_i32 s12, s13, s10
	global_load_lds_dwordx4 v[186:187], off
	v_lshl_add_u64 v[186:187], s[8:9], 0, v[164:165]
	s_mov_b32 m0, s12
	s_nop 0
	global_load_lds_dwordx4 v[186:187], off
	v_lshl_add_u64 v[186:187], s[8:9], 0, v[162:163]
	s_add_i32 m0, s12, 0x2000
	s_nop 0
	global_load_lds_dwordx4 v[186:187], off
	v_lshl_add_u64 v[186:187], v[216:217], 0, s[38:39]
	s_mov_b32 m0, s67
	s_nop 0
	global_load_lds_dwordx4 v[186:187], off
	v_lshl_add_u64 v[186:187], v[218:219], 0, s[38:39]
	s_mov_b32 m0, s78
	s_nop 0
	global_load_lds_dwordx4 v[186:187], off
	s_waitcnt vmcnt(8)
	s_waitcnt lgkmcnt(0)
	s_barrier
	s_setprio 1
	v_mfma_f32_16x16x32_bf16 v[62:65], v[130:133], v[174:177], v[62:65]
	v_mfma_f32_16x16x32_bf16 v[58:61], v[138:141], v[174:177], v[58:61]
	v_mfma_f32_16x16x32_bf16 v[54:57], v[130:133], v[182:185], v[54:57]
	v_mfma_f32_16x16x32_bf16 v[42:45], v[138:141], v[182:185], v[42:45]
	v_mfma_f32_16x16x32_bf16 v[38:41], v[130:133], v[198:201], v[38:41]
	v_mfma_f32_16x16x32_bf16 v[26:29], v[138:141], v[198:201], v[26:29]
	v_mfma_f32_16x16x32_bf16 v[22:25], v[130:133], v[206:209], v[22:25]
	v_mfma_f32_16x16x32_bf16 v[10:13], v[138:141], v[206:209], v[10:13]
	v_mfma_f32_16x16x32_bf16 v[62:65], v[134:137], v[178:181], v[62:65]
	v_mfma_f32_16x16x32_bf16 v[58:61], v[142:145], v[178:181], v[58:61]
	v_mfma_f32_16x16x32_bf16 v[54:57], v[134:137], v[194:197], v[54:57]
	v_mfma_f32_16x16x32_bf16 v[42:45], v[142:145], v[194:197], v[42:45]
	v_mfma_f32_16x16x32_bf16 v[38:41], v[134:137], v[202:205], v[38:41]
	v_mfma_f32_16x16x32_bf16 v[26:29], v[142:145], v[202:205], v[26:29]
	v_mfma_f32_16x16x32_bf16 v[22:25], v[134:137], v[210:213], v[22:25]
	v_mfma_f32_16x16x32_bf16 v[10:13], v[142:145], v[210:213], v[10:13]
	s_setprio 0
	s_setprio 1
	v_mfma_f32_16x16x32_bf16 v[50:53], v[146:149], v[174:177], v[50:53]
	v_mfma_f32_16x16x32_bf16 v[46:49], v[154:157], v[174:177], v[46:49]
	v_mfma_f32_16x16x32_bf16 v[34:37], v[146:149], v[182:185], v[34:37]
	v_mfma_f32_16x16x32_bf16 v[30:33], v[154:157], v[182:185], v[30:33]
	v_mfma_f32_16x16x32_bf16 v[18:21], v[146:149], v[198:201], v[18:21]
	v_mfma_f32_16x16x32_bf16 v[14:17], v[154:157], v[198:201], v[14:17]
	v_mfma_f32_16x16x32_bf16 v[6:9], v[146:149], v[206:209], v[6:9]
	v_mfma_f32_16x16x32_bf16 v[2:5], v[154:157], v[206:209], v[2:5]
	v_mfma_f32_16x16x32_bf16 v[50:53], v[150:153], v[178:181], v[50:53]
	v_mfma_f32_16x16x32_bf16 v[46:49], v[158:161], v[178:181], v[46:49]
	v_mfma_f32_16x16x32_bf16 v[34:37], v[150:153], v[194:197], v[34:37]
	v_mfma_f32_16x16x32_bf16 v[30:33], v[158:161], v[194:197], v[30:33]
	s_add_i32 s82, s82, 2
	s_add_u32 s60, s60, 0x100
	s_addc_u32 s61, s61, 0
	s_add_u32 s75, s75, 0x100
	s_addc_u32 s81, s81, 0
	s_cmp_gt_u32 s82, 29
	v_mfma_f32_16x16x32_bf16 v[18:21], v[150:153], v[202:205], v[18:21]
	v_mfma_f32_16x16x32_bf16 v[14:17], v[158:161], v[202:205], v[14:17]
	v_mfma_f32_16x16x32_bf16 v[6:9], v[150:153], v[210:213], v[6:9]
	v_mfma_f32_16x16x32_bf16 v[2:5], v[158:161], v[210:213], v[2:5]
	s_setprio 0
	s_barrier
	s_cbranch_scc0 .LBB0_469
	s_and_b64 vcc, exec, s[42:43]
	s_cbranch_vccz .LBB0_472
	s_barrier

; __device__ __forceinline__ v6u pk32_fp6(const float (&x)[32]) {
;     v16f a, b;
; #pragma unroll
;     for (int i = 0; i < 16; ++i) { a[i] = __builtin_amdgcn_fmed3f(x[i], -7.5f, 7.5f); b[i] = __builtin_amdgcn_fmed3f(x[16 + i], -7.5f, 7.5f); }
;     return __builtin_amdgcn_cvt_scalef32_2xpk16_fp6_f32(a, b, 1.0f);
; template <int MODE>
; __device__ __forceinline__ void tr_matrix6(const float* W, int nb, int K, int N, unsigned char* WT, int drows, int rot, int gw, int NGW, int lane, float wscale) {
;     ...
; #pragma unroll
;         for (int j = 0; j < 4; ++j) { float x[32];
; #pragma unroll
;             for (int i = 0; i < 32; ++i) x[i] = v[i][j] * wscale;
;             const v6u w = pk32_fp6(x);
;             *(u32x4*)(dst + (size_t)j * K) = (u32x4){w[0], w[1], w[2], w[3]}; *(u32x4*)(dst + (size_t)j * K + 16) = (u32x4){w[4], w[5], 0u, 0u}; }
.LBB0_1047:
	s_cmp_lg_u32 s100, 0
	s_cbranch_scc0 .Lf6_nostore
	s_and_b32 s18, s89, 2
	s_cmp_eq_u32 s18, 2
	s_cbranch_scc0 .Lf6_nostore
	s_mul_hi_u32 s18, s98, 0x2492493
	s_mul_i32 s19, s18, 0x70
	s_sub_u32 s19, s98, s19
	s_and_b32 s20, s18, 63
	s_lshr_b32 s18, s18, 6
	s_and_b32 s21, s18, 7
	s_lshr_b32 s18, s18, 3
	s_lshr_b32 s101, s19, 1
	s_lshl_b32 s101, s101, 8
	s_and_b32 s19, s19, 1
	s_lshl_b32 s19, s19, 6
	s_add_u32 s19, s19, s101
	s_lshl_b32 s18, s18, 7
	s_add_u32 s19, s19, s18
	s_mul_i32 s21, s21, 0x3800
	s_add_u32 s19, s19, s21
	s_lshl_b32 s19, s19, 11
	s_lshl_b32 s20, s20, 5
	s_add_u32 s19, s19, s20
	s_add_u32 s19, s19, 0x8a00000
	s_add_u32 s20, s70, s19
	s_addc_u32 s21, s71, 0
	v_mbcnt_lo_u32_b32 v218, -1, 0
	v_mbcnt_hi_u32_b32 v218, -1, v218
	v_lshlrev_b32_e32 v218, 11, v218
	v_mov_b32_e32 v219, 0x40f00000
	s_mov_b32 s18, 0x42b40000
	s_mov_b32 s19, 0x42b40000
	v_mov_b32_e32 v80, 0
	v_mov_b32_e32 v81, 0
	s_waitcnt vmcnt(0)
	v_pk_mul_f32 v[158:159], v[158:159], s[18:19]
	v_pk_mul_f32 v[160:161], v[160:161], s[18:19]
	v_pk_mul_f32 v[162:163], v[162:163], s[18:19]
	v_pk_mul_f32 v[164:165], v[164:165], s[18:19]
	v_pk_mul_f32 v[166:167], v[166:167], s[18:19]
	v_pk_mul_f32 v[168:169], v[168:169], s[18:19]
	v_pk_mul_f32 v[170:171], v[170:171], s[18:19]
	v_pk_mul_f32 v[172:173], v[172:173], s[18:19]
	v_pk_mul_f32 v[174:175], v[174:175], s[18:19]
	v_pk_mul_f32 v[176:177], v[176:177], s[18:19]
	v_pk_mul_f32 v[178:179], v[178:179], s[18:19]
	v_pk_mul_f32 v[180:181], v[180:181], s[18:19]
	v_pk_mul_f32 v[182:183], v[182:183], s[18:19]
	v_pk_mul_f32 v[184:185], v[184:185], s[18:19]
	v_pk_mul_f32 v[186:187], v[186:187], s[18:19]
	v_pk_mul_f32 v[188:189], v[188:189], s[18:19]
	s_mov_b32 s18, 0xc0f00000
	v_med3_f32 v158, v158, s18, v219
	v_med3_f32 v159, v159, s18, v219
	v_med3_f32 v160, v160, s18, v219
	v_med3_f32 v161, v161, s18, v219
	v_med3_f32 v162, v162, s18, v219
	v_med3_f32 v163, v163, s18, v219
	v_med3_f32 v164, v164, s18, v219
	v_med3_f32 v165, v165, s18, v219
	v_med3_f32 v166, v166, s18, v219
	v_med3_f32 v167, v167, s18, v219
	v_med3_f32 v168, v168, s18, v219
	v_med3_f32 v169, v169, s18, v219
	v_med3_f32 v170, v170, s18, v219
	v_med3_f32 v171, v171, s18, v219
	v_med3_f32 v172, v172, s18, v219
	v_med3_f32 v173, v173, s18, v219
	v_med3_f32 v174, v174, s18, v219
	v_med3_f32 v175, v175, s18, v219
	v_med3_f32 v176, v176, s18, v219
	v_med3_f32 v177, v177, s18, v219
	v_med3_f32 v178, v178, s18, v219
	v_med3_f32 v179, v179, s18, v219
	v_med3_f32 v180, v180, s18, v219
	v_med3_f32 v181, v181, s18, v219
	v_med3_f32 v182, v182, s18, v219
	v_med3_f32 v183, v183, s18, v219
	v_med3_f32 v184, v184, s18, v219
	v_med3_f32 v185, v185, s18, v219
	v_med3_f32 v186, v186, s18, v219
	v_med3_f32 v187, v187, s18, v219
	v_med3_f32 v188, v188, s18, v219
	v_med3_f32 v189, v189, s18, v219
	v_cvt_scalef32_2xpk16_fp6_f32 v[74:79], v[158:173], v[174:189], 1.0
	s_nop 1
	global_store_dwordx4 v218, v[74:77], s[20:21]
	global_store_dwordx4 v218, v[78:81], s[20:21] offset:16
	s_add_i32 s98, s98, 1
	s_mov_b32 s100, 0
